# p_mpost loop v2: one rstd chain for the four heads (lane groups carry the four sums, v_readlane broadcast) and next token's loads issued before the chain; arithmetic unchanged
# baseline (speedup 1.0000x reference)
.LBB0_1774:
	s_andn2_b64 vcc, exec, s[0:1]
	s_cbranch_vccnz .LBB0_1824
	v_readlane_b32 s0, v254, 9
	s_mov_b32 s0, -1
	v_readlane_b32 s14, v255, 0
	v_mbcnt_lo_u32_b32 v0, s0, 0
	v_mbcnt_hi_u32_b32 v0, s0, v0
	s_mov_b64 s[0:1], s[42:43]
	s_load_dwordx2 s[0:1], s[0:1], 0x68
	v_readlane_b32 s15, v255, 1
	s_add_u32 s7, s14, 0x49500000
	v_readlane_b32 s2, v254, 53
	s_addc_u32 s8, s15, 0
	s_lshl_b32 s2, s2, 12
	s_waitcnt vmcnt(0)
	v_and_b32_e32 v6, 63, v0
	s_waitcnt lgkmcnt(0)
	s_add_u32 s0, s0, s2
	s_addc_u32 s1, s1, 0
	v_lshlrev_b32_e32 v0, 4, v6
	v_lshl_add_u64 v[2:3], s[0:1], 0, v[0:1]
	v_and_b32_e32 v0, 64, v234
	v_add_u32_e32 v0, 64, v0
	v_xor_b32_e32 v5, 1, v234
	v_cmp_lt_i32_e32 vcc, v5, v0
	v_xor_b32_e32 v7, 2, v234
	s_mov_b32 s6, 0
	v_cndmask_b32_e32 v5, v234, v5, vcc
	v_cmp_lt_i32_e32 vcc, v7, v0
	v_lshlrev_b32_e32 v5, 2, v5
	v_readlane_b32 s9, v254, 49
	v_cndmask_b32_e32 v7, v234, v7, vcc
	v_lshlrev_b32_e32 v8, 2, v7
	v_xor_b32_e32 v7, 4, v234
	v_cmp_lt_i32_e32 vcc, v7, v0
	s_mov_b32 s12, 0xf800000
	v_readlane_b32 s3, v254, 54
	v_cndmask_b32_e32 v7, v234, v7, vcc
	v_lshlrev_b32_e32 v9, 2, v7
	v_xor_b32_e32 v7, 8, v234
	v_cmp_lt_i32_e32 vcc, v7, v0
	s_nop 1
	v_cndmask_b32_e32 v7, v234, v7, vcc
	v_lshlrev_b32_e32 v10, 2, v7
	v_xor_b32_e32 v7, 16, v234
	v_cmp_lt_i32_e32 vcc, v7, v0
	s_nop 1
	v_cndmask_b32_e32 v7, v234, v7, vcc
	v_lshlrev_b32_e32 v11, 2, v7
	v_xor_b32_e32 v7, 32, v234
	v_cmp_lt_i32_e32 vcc, v7, v0
	s_nop 1
	v_cndmask_b32_e32 v0, v234, v7, vcc
	v_lshlrev_b32_e32 v12, 2, v0
	v_lshlrev_b32_e32 v0, 3, v6
	v_cmp_lt_u32_e64 s[56:57], 15, v6
	v_cmp_lt_u32_e64 s[58:59], 31, v6
	v_cmp_lt_u32_e64 s[60:61], 47, v6
	s_add_i32 s0, s9, s6
	s_ashr_i32 s1, s0, 31
	s_lshl_b64 s[2:3], s[0:1], 11
	s_add_u32 s70, s7, s2
	s_addc_u32 s71, s8, s3
	s_mul_hi_i32 s1, s0, 0x5000
	s_mulk_i32 s0, 0x5000
	s_add_u32 s72, s14, s0
	s_addc_u32 s73, s15, s1
	s_add_u32 s72, s72, 0x33502680
	s_addc_u32 s73, s73, 0
	global_load_dwordx2 v[32:33], v0, s[70:71]
	global_load_dwordx2 v[34:35], v0, s[70:71] offset:512
	global_load_dwordx2 v[36:37], v0, s[70:71] offset:1024
	global_load_dwordx2 v[38:39], v0, s[70:71] offset:1536
	global_load_dwordx2 v[40:41], v0, s[72:73]
	global_load_dwordx2 v[42:43], v0, s[72:73] offset:512
	global_load_dwordx2 v[44:45], v0, s[72:73] offset:1024
	global_load_dwordx2 v[46:47], v0, s[72:73] offset:1536
	global_load_dwordx4 v[140:143], v[2:3], off
	global_load_dwordx4 v[144:147], v[2:3], off offset:1024
	global_load_dwordx4 v[148:151], v[2:3], off offset:2048
	global_load_dwordx4 v[152:155], v[2:3], off offset:3072
.LBB0_1776:
	s_add_i32 s0, s9, s6
	s_ashr_i32 s1, s0, 31
	s_lshl_b64 s[2:3], s[0:1], 11
	s_add_u32 s74, s21, s2
	s_addc_u32 s75, s26, s3
	s_waitcnt vmcnt(11)
	v_lshlrev_b32_e32 v48, 16, v32
	v_and_b32_e32 v49, 0xffff0000, v32
	v_lshlrev_b32_e32 v50, 16, v33
	v_and_b32_e32 v51, 0xffff0000, v33
	v_pk_mul_f32 v[18:19], v[48:49], v[48:49]
	v_pk_mul_f32 v[26:27], v[50:51], v[50:51]
	v_add_f32_e32 v112, v18, v19
	v_add_f32_e32 v112, v26, v112
	v_add_f32_e32 v112, v27, v112
	s_waitcnt vmcnt(10)
	v_lshlrev_b32_e32 v52, 16, v34
	v_and_b32_e32 v53, 0xffff0000, v34
	v_lshlrev_b32_e32 v54, 16, v35
	v_and_b32_e32 v55, 0xffff0000, v35
	v_pk_mul_f32 v[18:19], v[52:53], v[52:53]
	v_pk_mul_f32 v[26:27], v[54:55], v[54:55]
	v_add_f32_e32 v113, v18, v19
	v_add_f32_e32 v113, v26, v113
	v_add_f32_e32 v113, v27, v113
	s_waitcnt vmcnt(9)
	v_lshlrev_b32_e32 v56, 16, v36
	v_and_b32_e32 v57, 0xffff0000, v36
	v_lshlrev_b32_e32 v58, 16, v37
	v_and_b32_e32 v59, 0xffff0000, v37
	v_pk_mul_f32 v[18:19], v[56:57], v[56:57]
	v_pk_mul_f32 v[26:27], v[58:59], v[58:59]
	v_add_f32_e32 v114, v18, v19
	v_add_f32_e32 v114, v26, v114
	v_add_f32_e32 v114, v27, v114
	s_waitcnt vmcnt(8)
	v_lshlrev_b32_e32 v60, 16, v38
	v_and_b32_e32 v61, 0xffff0000, v38
	v_lshlrev_b32_e32 v62, 16, v39
	v_and_b32_e32 v63, 0xffff0000, v39
	v_pk_mul_f32 v[18:19], v[60:61], v[60:61]
	v_pk_mul_f32 v[26:27], v[62:63], v[62:63]
	v_add_f32_e32 v115, v18, v19
	v_add_f32_e32 v115, v26, v115
	v_add_f32_e32 v115, v27, v115
	ds_bpermute_b32 v116, v5, v112
	ds_bpermute_b32 v117, v5, v113
	ds_bpermute_b32 v118, v5, v114
	ds_bpermute_b32 v119, v5, v115
	s_waitcnt vmcnt(7)
	v_lshlrev_b32_e32 v13, 16, v40
	v_and_b32_e32 v30, 0xffff0000, v40
	v_lshlrev_b32_e32 v14, 16, v41
	v_and_b32_e32 v15, 0xffff0000, v41
	v_mul_f32_e32 v13, 0xbfb8aa3b, v13
	v_mul_f32_e32 v30, 0xbfb8aa3b, v30
	v_mul_f32_e32 v14, 0xbfb8aa3b, v14
	v_mul_f32_e32 v15, 0xbfb8aa3b, v15
	v_exp_f32_e32 v13, v13
	v_exp_f32_e32 v30, v30
	v_exp_f32_e32 v14, v14
	v_exp_f32_e32 v15, v15
	s_nop 0
	v_add_f32_e32 v13, 1.0, v13
	v_add_f32_e32 v30, 1.0, v30
	v_add_f32_e32 v14, 1.0, v14
	v_add_f32_e32 v15, 1.0, v15
	v_rcp_f32_e32 v96, v13
	v_rcp_f32_e32 v97, v30
	v_rcp_f32_e32 v98, v14
	v_rcp_f32_e32 v99, v15
	s_waitcnt lgkmcnt(0)
	v_add_f32_e32 v112, v112, v116
	v_add_f32_e32 v113, v113, v117
	v_add_f32_e32 v114, v114, v118
	v_add_f32_e32 v115, v115, v119
	ds_bpermute_b32 v116, v8, v112
	ds_bpermute_b32 v117, v8, v113
	ds_bpermute_b32 v118, v8, v114
	ds_bpermute_b32 v119, v8, v115
	s_waitcnt vmcnt(6)
	v_lshlrev_b32_e32 v13, 16, v42
	v_and_b32_e32 v30, 0xffff0000, v42
	v_lshlrev_b32_e32 v14, 16, v43
	v_and_b32_e32 v15, 0xffff0000, v43
	v_mul_f32_e32 v13, 0xbfb8aa3b, v13
	v_mul_f32_e32 v30, 0xbfb8aa3b, v30
	v_mul_f32_e32 v14, 0xbfb8aa3b, v14
	v_mul_f32_e32 v15, 0xbfb8aa3b, v15
	v_exp_f32_e32 v13, v13
	v_exp_f32_e32 v30, v30
	v_exp_f32_e32 v14, v14
	v_exp_f32_e32 v15, v15
	s_nop 0
	v_add_f32_e32 v13, 1.0, v13
	v_add_f32_e32 v30, 1.0, v30
	v_add_f32_e32 v14, 1.0, v14
	v_add_f32_e32 v15, 1.0, v15
	v_rcp_f32_e32 v100, v13
	v_rcp_f32_e32 v101, v30
	v_rcp_f32_e32 v102, v14
	v_rcp_f32_e32 v103, v15
	s_waitcnt lgkmcnt(0)
	v_add_f32_e32 v112, v112, v116
	v_add_f32_e32 v113, v113, v117
	v_add_f32_e32 v114, v114, v118
	v_add_f32_e32 v115, v115, v119
	ds_bpermute_b32 v116, v9, v112
	ds_bpermute_b32 v117, v9, v113
	ds_bpermute_b32 v118, v9, v114
	ds_bpermute_b32 v119, v9, v115
	s_waitcnt vmcnt(5)
	v_lshlrev_b32_e32 v13, 16, v44
	v_and_b32_e32 v30, 0xffff0000, v44
	v_lshlrev_b32_e32 v14, 16, v45
	v_and_b32_e32 v15, 0xffff0000, v45
	v_mul_f32_e32 v13, 0xbfb8aa3b, v13
	v_mul_f32_e32 v30, 0xbfb8aa3b, v30
	v_mul_f32_e32 v14, 0xbfb8aa3b, v14
	v_mul_f32_e32 v15, 0xbfb8aa3b, v15
	v_exp_f32_e32 v13, v13
	v_exp_f32_e32 v30, v30
	v_exp_f32_e32 v14, v14
	v_exp_f32_e32 v15, v15
	s_nop 0
	v_add_f32_e32 v13, 1.0, v13
	v_add_f32_e32 v30, 1.0, v30
	v_add_f32_e32 v14, 1.0, v14
	v_add_f32_e32 v15, 1.0, v15
	v_rcp_f32_e32 v104, v13
	v_rcp_f32_e32 v105, v30
	v_rcp_f32_e32 v106, v14
	v_rcp_f32_e32 v107, v15
	s_waitcnt lgkmcnt(0)
	v_add_f32_e32 v112, v112, v116
	v_add_f32_e32 v113, v113, v117
	v_add_f32_e32 v114, v114, v118
	v_add_f32_e32 v115, v115, v119
	ds_bpermute_b32 v116, v10, v112
	ds_bpermute_b32 v117, v10, v113
	ds_bpermute_b32 v118, v10, v114
	ds_bpermute_b32 v119, v10, v115
	s_waitcnt vmcnt(4)
	v_lshlrev_b32_e32 v13, 16, v46
	v_and_b32_e32 v30, 0xffff0000, v46
	v_lshlrev_b32_e32 v14, 16, v47
	v_and_b32_e32 v15, 0xffff0000, v47
	v_mul_f32_e32 v13, 0xbfb8aa3b, v13
	v_mul_f32_e32 v30, 0xbfb8aa3b, v30
	v_mul_f32_e32 v14, 0xbfb8aa3b, v14
	v_mul_f32_e32 v15, 0xbfb8aa3b, v15
	v_exp_f32_e32 v13, v13
	v_exp_f32_e32 v30, v30
	v_exp_f32_e32 v14, v14
	v_exp_f32_e32 v15, v15
	s_nop 0
	v_add_f32_e32 v13, 1.0, v13
	v_add_f32_e32 v30, 1.0, v30
	v_add_f32_e32 v14, 1.0, v14
	v_add_f32_e32 v15, 1.0, v15
	v_rcp_f32_e32 v108, v13
	v_rcp_f32_e32 v109, v30
	v_rcp_f32_e32 v110, v14
	v_rcp_f32_e32 v111, v15
	s_waitcnt lgkmcnt(0)
	v_add_f32_e32 v112, v112, v116
	v_add_f32_e32 v113, v113, v117
	v_add_f32_e32 v114, v114, v118
	v_add_f32_e32 v115, v115, v119
	ds_bpermute_b32 v116, v11, v112
	ds_bpermute_b32 v117, v11, v113
	ds_bpermute_b32 v118, v11, v114
	ds_bpermute_b32 v119, v11, v115
	s_waitcnt lgkmcnt(0)
	v_add_f32_e32 v112, v112, v116
	v_add_f32_e32 v113, v113, v117
	v_add_f32_e32 v114, v114, v118
	v_add_f32_e32 v115, v115, v119
	ds_bpermute_b32 v116, v12, v112
	ds_bpermute_b32 v117, v12, v113
	ds_bpermute_b32 v118, v12, v114
	ds_bpermute_b32 v119, v12, v115
	s_waitcnt lgkmcnt(0)
	v_add_f32_e32 v112, v112, v116
	v_add_f32_e32 v113, v113, v117
	v_add_f32_e32 v114, v114, v118
	v_add_f32_e32 v115, v115, v119
	s_addk_i32 s6, 0x100
	s_cmpk_eq_i32 s6, 0x800
	s_cbranch_scc1 .Lmp_nopf
	s_add_i32 s0, s9, s6
	s_ashr_i32 s1, s0, 31
	s_lshl_b64 s[2:3], s[0:1], 11
	s_add_u32 s70, s7, s2
	s_addc_u32 s71, s8, s3
	s_mul_hi_i32 s1, s0, 0x5000
	s_mulk_i32 s0, 0x5000
	s_add_u32 s72, s14, s0
	s_addc_u32 s73, s15, s1
	s_add_u32 s72, s72, 0x33502680
	s_addc_u32 s73, s73, 0
	global_load_dwordx2 v[32:33], v0, s[70:71]
	global_load_dwordx2 v[34:35], v0, s[70:71] offset:512
	global_load_dwordx2 v[36:37], v0, s[70:71] offset:1024
	global_load_dwordx2 v[38:39], v0, s[70:71] offset:1536
	global_load_dwordx2 v[40:41], v0, s[72:73]
	global_load_dwordx2 v[42:43], v0, s[72:73] offset:512
	global_load_dwordx2 v[44:45], v0, s[72:73] offset:1024
	global_load_dwordx2 v[46:47], v0, s[72:73] offset:1536
.Lmp_nopf:
	v_cndmask_b32_e64 v13, v112, v113, s[56:57]
	v_cndmask_b32_e64 v13, v13, v114, s[58:59]
	v_cndmask_b32_e64 v13, v13, v115, s[60:61]
	v_fmamk_f32 v13, v13, 0x3b800000, v230
	v_cmp_gt_f32_e32 vcc, s12, v13
	v_mul_f32_e32 v18, 0x4f800000, v13
	s_nop 0
	v_cndmask_b32_e32 v13, v13, v18, vcc
	v_sqrt_f32_e32 v18, v13
	s_nop 0
	v_add_u32_e32 v19, -1, v18
	v_fma_f32 v26, -v19, v18, v13
	v_cmp_ge_f32_e64 s[2:3], 0, v26
	v_add_u32_e32 v26, 1, v18
	s_nop 0
	v_cndmask_b32_e64 v19, v18, v19, s[2:3]
	v_fma_f32 v18, -v26, v18, v13
	v_cmp_lt_f32_e64 s[2:3], 0, v18
	s_nop 1
	v_cndmask_b32_e64 v18, v19, v26, s[2:3]
	v_mul_f32_e32 v19, 0x37800000, v18
	v_cndmask_b32_e32 v18, v18, v19, vcc
	v_cmp_class_f32_e32 vcc, v13, v231
	s_nop 1
	v_cndmask_b32_e32 v13, v18, v13, vcc
	v_div_scale_f32 v18, s[2:3], v13, v13, 1.0
	v_rcp_f32_e32 v19, v18
	s_nop 0
	v_fma_f32 v26, -v18, v19, 1.0
	v_fmac_f32_e32 v19, v26, v19
	v_div_scale_f32 v26, vcc, 1.0, v13, 1.0
	v_mul_f32_e32 v27, v26, v19
	v_fma_f32 v30, -v18, v27, v26
	v_fmac_f32_e32 v27, v30, v19
	v_fma_f32 v18, -v18, v27, v26
	v_div_fmas_f32 v18, v18, v19, v27
	v_div_fixup_f32 v18, v18, v13, 1.0
	s_nop 0
	v_readlane_b32 s62, v18, 0
	v_readlane_b32 s64, v18, 16
	v_readlane_b32 s66, v18, 32
	v_readlane_b32 s68, v18, 48
	s_nop 1
	s_waitcnt vmcnt(8)
	v_pk_mul_f32 v[156:157], s[62:63], v[48:49] op_sel_hi:[0,1]
	v_pk_mul_f32 v[158:159], s[62:63], v[50:51] op_sel_hi:[0,1]
	v_pk_mul_f32 v[156:157], v[140:141], v[156:157]
	v_pk_mul_f32 v[158:159], v[142:143], v[158:159]
	v_pk_mul_f32 v[156:157], v[96:97], v[156:157]
	v_pk_mul_f32 v[158:159], v[98:99], v[158:159]
	v_cvt_pk_bf16_f32 v156, v156, v157
	v_cvt_pk_bf16_f32 v157, v158, v159
	global_store_dwordx2 v0, v[156:157], s[74:75]
	v_pk_mul_f32 v[160:161], s[64:65], v[52:53] op_sel_hi:[0,1]
	v_pk_mul_f32 v[162:163], s[64:65], v[54:55] op_sel_hi:[0,1]
	v_pk_mul_f32 v[160:161], v[144:145], v[160:161]
	v_pk_mul_f32 v[162:163], v[146:147], v[162:163]
	v_pk_mul_f32 v[160:161], v[100:101], v[160:161]
	v_pk_mul_f32 v[162:163], v[102:103], v[162:163]
	v_cvt_pk_bf16_f32 v160, v160, v161
	v_cvt_pk_bf16_f32 v161, v162, v163
	global_store_dwordx2 v0, v[160:161], s[74:75] offset:512
	v_pk_mul_f32 v[164:165], s[66:67], v[56:57] op_sel_hi:[0,1]
	v_pk_mul_f32 v[166:167], s[66:67], v[58:59] op_sel_hi:[0,1]
	v_pk_mul_f32 v[164:165], v[148:149], v[164:165]
	v_pk_mul_f32 v[166:167], v[150:151], v[166:167]
	v_pk_mul_f32 v[164:165], v[104:105], v[164:165]
	v_pk_mul_f32 v[166:167], v[106:107], v[166:167]
	v_cvt_pk_bf16_f32 v164, v164, v165
	v_cvt_pk_bf16_f32 v165, v166, v167
	global_store_dwordx2 v0, v[164:165], s[74:75] offset:1024
	v_pk_mul_f32 v[168:169], s[68:69], v[60:61] op_sel_hi:[0,1]
	v_pk_mul_f32 v[170:171], s[68:69], v[62:63] op_sel_hi:[0,1]
	v_pk_mul_f32 v[168:169], v[152:153], v[168:169]
	v_pk_mul_f32 v[170:171], v[154:155], v[170:171]
	v_pk_mul_f32 v[168:169], v[108:109], v[168:169]
	v_pk_mul_f32 v[170:171], v[110:111], v[170:171]
	v_cvt_pk_bf16_f32 v168, v168, v169
	v_cvt_pk_bf16_f32 v169, v170, v171
	global_store_dwordx2 v0, v[168:169], s[74:75] offset:1536
	s_cmpk_lg_i32 s6, 0x800
	s_cbranch_scc1 .LBB0_1776
	v_readlane_b32 s0, v254, 57
	s_add_i32 s20, s0, 8
	v_readlane_b32 s0, v254, 5
	s_cmp_ge_i32 s20, s0
	s_cbranch_scc1 .LBB0_1824
	v_readlane_b32 s0, v254, 9
	s_waitcnt vmcnt(0)
	s_barrier
	s_mov_b32 s1, -1
	s_lshl_b32 s0, s0, 6
	v_mbcnt_lo_u32_b32 v0, s1, 0
	v_mbcnt_hi_u32_b32 v0, s1, v0
	s_sub_i32 s0, 0, s0
	v_cmp_eq_u32_e32 vcc, s0, v0
	s_and_saveexec_b64 s[0:1], vcc
	s_cbranch_execz .LBB0_1823
	v_readlane_b32 s2, v254, 6
	v_readlane_b32 s4, v254, 8
	v_readlane_b32 s3, v254, 7
	s_waitcnt vmcnt(0) expcnt(0) lgkmcnt(0)
	v_mov_b32_e32 v0, s4
	ds_read_b32 v2, v0
	ds_read_b32 v0, v0 offset:4
	s_waitcnt lgkmcnt(1)
	v_cmp_ne_u32_e32 vcc, 0, v2
	s_cbranch_vccnz .LBB0_1793
	s_add_u32 s4, s2, 0x1000
	s_addc_u32 s5, s3, 0
	s_add_u32 s6, s2, 0x1100
	s_addc_u32 s7, s3, 0
	s_add_u32 s8, s2, 0x1200
	s_addc_u32 s9, s3, 0
	s_add_u32 s10, s2, 0x1300
	s_addc_u32 s11, s3, 0
	s_mov_b32 s38, 1
	s_mov_b64 s[12:13], 0
	s_branch .LBB0_1783
